# scan
# baseline (speedup 1.0000x reference)
.LBB0_30:
	s_andn2_saveexec_b64 s[4:5], s[10:11]
	v_mov_b32_e32 v13, 0.5
	v_fmamk_f32 v13, v14, 0xbeaaaaab, v13
	v_fma_f32 v13, -v14, v13, 1.0
	v_mul_f32_e32 v13, v14, v13
	s_or_b64 exec, exec, s[4:5]
	v_max_f32_e32 v10, v10, v10
	v_max_f32_e32 v10, 0, v10
	v_add_f32_e32 v10, v10, v12
	s_waitcnt vmcnt(3)
	v_mul_f32_e32 v9, v9, v10
	v_mul_f32_e32 v10, 0x41c80000, v9
	s_mov_b32 s3, 0x3c23d70a
	v_cmp_ngt_f32_e32 vcc, s3, v10
	s_and_saveexec_b64 s[4:5], vcc
	s_xor_b64 s[4:5], exec, s[4:5]
	v_mul_f32_e32 v9, 0xbfb8aa3b, v10
	v_exp_f32_e32 v9, v9
	s_nop 0
	v_sub_f32_e32 v9, 1.0, v9
	s_andn2_saveexec_b64 s[4:5], s[4:5]
	v_mov_b32_e32 v9, 0.5
	v_fmamk_f32 v9, v10, 0xbe2aaaab, v9
	v_fma_f32 v9, -v10, v9, 1.0
	v_mul_f32_e32 v9, v10, v9
	s_or_b64 exec, exec, s[4:5]
	v_max_f32_e32 v10, v11, v11
	v_max_f32_e32 v10, 0, v10
	v_add_f32_e32 v10, v10, v13
	s_waitcnt vmcnt(2)
	v_mul_f32_e32 v8, v8, v10
	v_mul_f32_e32 v10, 0x41c80000, v8
	v_cmp_ngt_f32_e32 vcc, s3, v10
	s_and_saveexec_b64 s[4:5], vcc
	s_xor_b64 s[4:5], exec, s[4:5]
	v_mul_f32_e32 v8, 0xbfb8aa3b, v10
	v_exp_f32_e32 v8, v8
	s_nop 0
	v_sub_f32_e32 v8, 1.0, v8
	s_andn2_saveexec_b64 s[4:5], s[4:5]
	v_mov_b32_e32 v8, 0.5
	v_fmamk_f32 v8, v10, 0xbe2aaaab, v8
	v_fma_f32 v8, -v10, v8, 1.0
	v_mul_f32_e32 v8, v10, v8
	s_or_b64 exec, exec, s[4:5]
	v_cmp_eq_u32_e32 vcc, 63, v7
	v_mov_b32_e32 v12, 1.0
	v_mov_b32_e32 v11, 1.0
	v_cndmask_b32_e64 v7, v8, 1.0, vcc
	v_sub_f32_e32 v8, 1.0, v9
	v_add_f32_e32 v8, 0x2edbe6ff, v8
	v_sub_f32_e32 v10, 1.0, v7
	v_add_f32_e32 v10, 0x2edbe6ff, v10
	v_lshl_add_u64 v[4:5], v[4:5], 2, s[6:7]
	s_mov_b64 s[4:5], 0x216000
	v_mov_b32_e32 v12, 1.0
	v_mov_b32_e32 v64, 1.0
	v_mov_b32_dpp v12, v8 row_shr:1 row_mask:0xf bank_mask:0xf
	v_mov_b32_dpp v64, v10 row_shr:1 row_mask:0xf bank_mask:0xf
	v_mul_f32_e32 v8, v8, v12
	v_mul_f32_e32 v10, v10, v64
	v_mov_b32_e32 v12, 1.0
	v_mov_b32_e32 v64, 1.0
	v_mov_b32_dpp v12, v8 row_shr:2 row_mask:0xf bank_mask:0xf
	v_mov_b32_dpp v64, v10 row_shr:2 row_mask:0xf bank_mask:0xf
	v_mul_f32_e32 v8, v8, v12
	v_mul_f32_e32 v10, v10, v64
	v_mov_b32_e32 v12, 1.0
	v_mov_b32_e32 v64, 1.0
	v_mov_b32_dpp v12, v8 row_shr:4 row_mask:0xf bank_mask:0xf
	v_mov_b32_dpp v64, v10 row_shr:4 row_mask:0xf bank_mask:0xf
	v_mul_f32_e32 v8, v8, v12
	v_mul_f32_e32 v10, v10, v64
	v_mov_b32_e32 v12, 1.0
	v_mov_b32_e32 v64, 1.0
	v_mov_b32_dpp v12, v8 row_shr:8 row_mask:0xf bank_mask:0xf
	v_mov_b32_dpp v64, v10 row_shr:8 row_mask:0xf bank_mask:0xf
	v_mul_f32_e32 v8, v8, v12
	v_mul_f32_e32 v10, v10, v64
	v_mov_b32_e32 v12, 1.0
	v_mov_b32_e32 v64, 1.0
	v_mov_b32_dpp v12, v8 row_bcast:15 row_mask:0xa bank_mask:0xf
	v_mov_b32_dpp v64, v10 row_bcast:15 row_mask:0xa bank_mask:0xf
	v_mul_f32_e32 v8, v8, v12
	v_mul_f32_e32 v10, v10, v64
	v_mov_b32_e32 v12, 1.0
	v_mov_b32_e32 v64, 1.0
	v_mov_b32_dpp v12, v8 row_bcast:31 row_mask:0xc bank_mask:0xf
	v_mov_b32_dpp v64, v10 row_bcast:31 row_mask:0xc bank_mask:0xf
	v_mul_f32_e32 v8, v8, v12
	v_mul_f32_e32 v10, v10, v64
	v_mov_b32_e32 v12, 1.0
	v_mov_b32_e32 v64, 1.0
	v_readlane_b32 s3, v8, 63
	v_mov_b32_dpp v11, v10 wave_shr:1 row_mask:0xf bank_mask:0xf
	v_mov_b32_dpp v12, v8 wave_shr:1 row_mask:0xf bank_mask:0xf
	v_mul_f32_e32 v10, s3, v11
	s_mov_b32 s3, 0x216000
	v_mul_f32_e32 v13, v7, v10
	v_lshl_add_u64 v[10:11], v[4:5], 0, s[4:5]
	v_add_co_u32_e64 v4, s[4:5], s3, v4
	v_mul_f32_e32 v8, v9, v12
	s_nop 0
	v_addc_co_u32_e64 v5, s[4:5], 0, v5, s[4:5]
	s_waitcnt vmcnt(0)
	v_mul_f32_e32 v6, v6, v13
	global_store_dword v[4:5], v8, off
	global_store_dword v[10:11], v13, off offset:256
	v_fma_f32 v5, v9, v12, v13
	v_fmac_f32_e32 v6, v1, v8
	v_mov_b32_e32 v7, 0
	v_add_f32_dpp v5, v5, v5 row_shr:1 row_mask:0xf bank_mask:0xf bound_ctrl:1
	v_add_f32_dpp v1, v6, v6 row_shr:1 row_mask:0xf bank_mask:0xf bound_ctrl:1
	v_mov_b32_e32 v6, 0
	v_add_f32_dpp v5, v5, v5 row_shr:2 row_mask:0xf bank_mask:0xf bound_ctrl:1
	v_add_f32_dpp v1, v1, v1 row_shr:2 row_mask:0xf bank_mask:0xf bound_ctrl:1
	v_mov_b32_e32 v4, 0
	v_add_f32_dpp v5, v5, v5 row_shr:4 row_mask:0xf bank_mask:0xf bound_ctrl:1
	v_add_f32_dpp v1, v1, v1 row_shr:4 row_mask:0xf bank_mask:0xf bound_ctrl:1
	s_nop 0
	v_add_f32_dpp v5, v5, v5 row_shr:8 row_mask:0xf bank_mask:0xf bound_ctrl:1
	v_add_f32_dpp v1, v1, v1 row_shr:8 row_mask:0xf bank_mask:0xf bound_ctrl:1
	s_nop 0
	v_mov_b32_dpp v7, v5 row_bcast:15 row_mask:0xa bank_mask:0xf
	v_mov_b32_dpp v6, v1 row_bcast:15 row_mask:0xa bank_mask:0xf
	v_add_f32_e32 v5, v5, v7
	v_mov_b32_e32 v7, 0
	v_add_f32_e32 v1, v1, v6
	s_nop 0
	v_mov_b32_dpp v7, v5 row_bcast:31 row_mask:0xc bank_mask:0xf
	v_mov_b32_dpp v4, v1 row_bcast:31 row_mask:0xc bank_mask:0xf
	s_and_saveexec_b64 s[4:5], vcc
	s_cbranch_execz .LBB0_42
	s_load_dwordx2 s[10:11], s[0:1], 0x48
	v_add_f32_e32 v1, v1, v4
	v_add_f32_e32 v6, v5, v7
	s_waitcnt lgkmcnt(0)
	v_lshl_add_u64 v[2:3], v[2:3], 2, s[10:11]
	v_add_co_u32_e32 v4, vcc, 0xc000, v2
	s_nop 1
	v_addc_co_u32_e32 v5, vcc, 0, v3, vcc
	v_add_co_u32_e32 v2, vcc, 0x10000, v2
	global_store_dword v[4:5], v1, off
	s_nop 0
	v_addc_co_u32_e32 v3, vcc, 0, v3, vcc
	global_store_dword v[2:3], v6, off
